# speedup vs baseline: 1.1017x; 1.0363x over previous
.LBB0_20:
	s_or_b64 exec, exec, s[0:1]
	v_lshrrev_b32_e32 v12, 6, v0
	v_bfe_u32 v131, v0, 4, 2
	v_and_b32_e32 v106, 15, v0
	v_lshlrev_b32_e32 v107, 5, v12
	v_or_b32_e32 v73, v107, v106
	v_lshlrev_b32_e32 v60, 5, v131
	v_mov_b32_e32 v61, 0
	v_lshl_add_u64 v[42:43], s[30:31], 0, v[60:61]
	v_lshlrev_b32_e32 v2, 7, v73
	v_mov_b32_e32 v3, v61
	v_lshl_add_u64 v[10:11], v[42:43], 0, v[2:3]
	v_lshl_add_u64 v[50:51], s[18:19], 0, v[60:61]
	global_load_dwordx4 v[2:5], v[10:11], off offset:16
	global_load_dwordx4 v[6:9], v[10:11], off
	v_lshlrev_b32_e32 v10, 9, v73
	v_mov_b32_e32 v11, v61
	v_lshl_add_u64 v[34:35], v[50:51], 0, v[10:11]
	v_lshlrev_b32_e32 v62, 7, v12
	v_mov_b32_e32 v63, v61
	v_lshl_add_u64 v[18:19], v[34:35], 0, v[62:63]
	global_load_dwordx4 v[10:13], v[18:19], off offset:16
	global_load_dwordx4 v[14:17], v[18:19], off
	v_add_u32_e32 v18, 32, v107
	v_and_b32_e32 v108, 0x60, v18
	v_lshlrev_b32_e32 v64, 2, v108
	v_mov_b32_e32 v65, v61
	v_lshl_add_u64 v[26:27], v[34:35], 0, v[64:65]
	v_xor_b32_e32 v109, 64, v107
	global_load_dwordx4 v[18:21], v[26:27], off offset:16
	global_load_dwordx4 v[22:25], v[26:27], off
	v_lshlrev_b32_e32 v66, 2, v109
	v_mov_b32_e32 v67, v61
	v_lshl_add_u64 v[36:37], v[34:35], 0, v[66:67]
	global_load_dwordx4 v[26:29], v[36:37], off
	global_load_dwordx4 v[30:33], v[36:37], off offset:16
	v_add_u32_e32 v36, 0x60, v107
	v_and_b32_e32 v111, 0x60, v36
	v_mov_b32_e32 v69, v61
	v_lshlrev_b32_e32 v68, 2, v111
	v_lshl_add_u64 v[44:45], v[34:35], 0, v[68:69]
	global_load_dwordx4 v[34:37], v[44:45], off
	global_load_dwordx4 v[38:41], v[44:45], off offset:16
	v_or_b32_e32 v54, 16, v73
	v_mov_b32_e32 v45, v61
	v_lshlrev_b32_e32 v44, 7, v54
	v_lshl_add_u64 v[52:53], v[42:43], 0, v[44:45]
	global_load_dwordx4 v[42:45], v[52:53], off
	global_load_dwordx4 v[46:49], v[52:53], off offset:16
	v_mov_b32_e32 v53, v61
	v_lshlrev_b32_e32 v52, 9, v54
	v_lshl_add_u64 v[58:59], v[50:51], 0, v[52:53]
	v_lshl_add_u64 v[70:71], v[58:59], 0, v[62:63]
	global_load_dwordx4 v[50:53], v[70:71], off
	global_load_dwordx4 v[54:57], v[70:71], off offset:16
	v_lshl_add_u64 v[70:71], v[58:59], 0, v[64:65]
	v_lshl_add_u64 v[98:99], v[58:59], 0, v[66:67]
	v_lshl_add_u64 v[58:59], v[58:59], 0, v[68:69]
	global_load_dwordx4 v[74:77], v[70:71], off offset:16
	global_load_dwordx4 v[78:81], v[70:71], off
	global_load_dwordx4 v[82:85], v[98:99], off offset:16
	global_load_dwordx4 v[86:89], v[98:99], off
	global_load_dwordx4 v[90:93], v[58:59], off offset:16
	global_load_dwordx4 v[94:97], v[58:59], off
	s_mov_b32 s0, 0x3fb8aa3b
	v_lshlrev_b32_e32 v72, 9, v0
	v_and_b32_e32 v1, 16, v1
	v_or3_b32 v107, v106, v1, v107
	v_lshlrev_b32_e32 v107, 1, v107
	s_mov_b32 s3, 32
	v_cmp_eq_u32_e64 s[4:5], 3, v131
	s_waitcnt vmcnt(19)
	v_pk_mul_f32 v[58:59], v[2:3], s[0:1] op_sel_hi:[1,0]
	s_waitcnt vmcnt(18)
	v_pk_mul_f32 v[6:7], v[6:7], s[0:1] op_sel_hi:[1,0]
	v_pk_mul_f32 v[8:9], v[8:9], s[0:1] op_sel_hi:[1,0]
	v_cvt_pk_f16_f32 v2, v6, v7
	v_cvt_pk_f16_f32 v3, v8, v9
	v_pk_mul_f32 v[70:71], v[4:5], s[0:1] op_sel_hi:[1,0]
	v_cvt_pk_f16_f32 v4, v58, v59
	s_waitcnt vmcnt(17)
	v_cvt_f16_f32_e32 v13, v13
	s_waitcnt vmcnt(16)
	v_cvt_f16_f32_e32 v6, v14
	v_cvt_pk_f16_f32 v8, v17, v10
	v_cvt_pk_f16_f32 v5, v70, v71
	v_lshl_add_u64 v[70:71], s[22:23], 0, v[60:61]
	v_and_b32_e32 v60, 0x19e00, v72
	v_cvt_pk_f16_f32 v9, v15, v16
	s_waitcnt vmcnt(15)
	v_cvt_f16_f32_e32 v17, v21
	v_cvt_pk_f16_f32 v10, v11, v12
	s_waitcnt vmcnt(14)
	v_cvt_f16_f32_e32 v14, v22
	v_cvt_pk_f16_f32 v15, v23, v24
	v_cvt_pk_f16_f32 v12, v25, v18
	v_cvt_pk_f16_f32 v16, v19, v20
	v_lshl_add_u64 v[58:59], v[70:71], 0, v[60:61]
	s_waitcnt vmcnt(13)
	v_cvt_f16_f32_e32 v18, v26
	v_alignbit_b32 v7, v8, v9, 16
	v_alignbit_b32 v11, v12, v15, 16
	v_alignbit_b32 v12, v16, v12, 16
	v_pack_b32_f16 v6, v6, v9
	v_alignbit_b32 v9, v13, v10, 16
	v_alignbit_b32 v13, v17, v16, 16
	v_lshl_add_u64 v[16:17], v[58:59], 0, v[62:63]
	global_load_dwordx4 v[98:101], v[16:17], off offset:16
	global_load_dwordx4 v[102:105], v[16:17], off
	s_waitcnt vmcnt(14)
	v_cvt_f16_f32_e32 v17, v33
	s_waitcnt vmcnt(13)
	v_cvt_f16_f32_e32 v20, v34
	v_alignbit_b32 v8, v10, v8, 16
	v_pack_b32_f16 v10, v14, v15
	v_cvt_pk_f16_f32 v15, v27, v28
	v_pack_b32_f16 v14, v18, v15
	v_cvt_pk_f16_f32 v18, v29, v30
	v_cvt_pk_f16_f32 v19, v31, v32
	v_alignbit_b32 v16, v19, v18, 16
	v_alignbit_b32 v17, v17, v19, 16
	v_cvt_pk_f16_f32 v19, v35, v36
	v_alignbit_b32 v15, v18, v15, 16
	v_pack_b32_f16 v18, v20, v19
	v_lshl_add_u64 v[20:21], v[58:59], 0, v[64:65]
	global_load_dwordx4 v[112:115], v[20:21], off offset:16
	global_load_dwordx4 v[116:119], v[20:21], off
	s_waitcnt vmcnt(14)
	v_cvt_f16_f32_e32 v21, v41
	v_lshl_add_u64 v[26:27], v[58:59], 0, v[66:67]
	global_load_dwordx4 v[124:127], v[26:27], off offset:16
	global_load_dwordx4 v[132:135], v[26:27], off
	v_cvt_pk_f16_f32 v20, v37, v38
	v_cvt_pk_f16_f32 v22, v39, v40
	s_waitcnt vmcnt(13)
	v_cvt_f16_f32_e32 v28, v50
	v_alignbit_b32 v19, v20, v19, 16
	v_alignbit_b32 v20, v22, v20, 16
	v_alignbit_b32 v21, v21, v22, 16
	v_pk_mul_f32 v[22:23], v[42:43], s[0:1] op_sel_hi:[1,0]
	v_pk_mul_f32 v[24:25], v[44:45], s[0:1] op_sel_hi:[1,0]
	v_cvt_pk_f16_f32 v22, v22, v23
	v_cvt_pk_f16_f32 v23, v24, v25
	v_pk_mul_f32 v[24:25], v[46:47], s[0:1] op_sel_hi:[1,0]
	v_pk_mul_f32 v[26:27], v[48:49], s[0:1] op_sel_hi:[1,0]
	v_cvt_pk_f16_f32 v24, v24, v25
	v_cvt_pk_f16_f32 v25, v26, v27
	v_cvt_pk_f16_f32 v27, v51, v52
	s_waitcnt vmcnt(12)
	v_cvt_f16_f32_e32 v31, v57
	v_pack_b32_f16 v26, v28, v27
	v_lshl_add_u64 v[28:29], v[58:59], 0, v[68:69]
	global_load_dwordx4 v[140:143], v[28:29], off offset:16
	global_load_dwordx4 v[144:147], v[28:29], off
	s_mov_b64 s[0:1], 0x2000
	v_cvt_pk_f16_f32 v30, v53, v54
	v_cvt_pk_f16_f32 v29, v55, v56
	v_lshl_add_u64 v[46:47], v[58:59], 0, s[0:1]
	v_alignbit_b32 v27, v30, v27, 16
	v_alignbit_b32 v28, v29, v30, 16
	v_alignbit_b32 v29, v31, v29, 16
	v_lshl_add_u64 v[30:31], v[46:47], 0, v[62:63]
	global_load_dwordx4 v[148:151], v[30:31], off offset:16
	global_load_dwordx4 v[152:155], v[30:31], off
	s_waitcnt vmcnt(14)
	v_cvt_f16_f32_e32 v32, v78
	v_cvt_f16_f32_e32 v33, v77
	s_waitcnt vmcnt(12)
	v_cvt_f16_f32_e32 v35, v86
	v_cvt_pk_f16_f32 v31, v79, v80
	v_pack_b32_f16 v30, v32, v31
	v_cvt_pk_f16_f32 v32, v81, v74
	v_cvt_pk_f16_f32 v34, v75, v76
	v_cvt_pk_f16_f32 v36, v87, v88
	v_cvt_pk_f16_f32 v38, v89, v82
	v_alignbit_b32 v31, v32, v31, 16
	v_alignbit_b32 v32, v34, v32, 16
	v_alignbit_b32 v33, v33, v34, 16
	v_pack_b32_f16 v34, v35, v36
	v_alignbit_b32 v35, v38, v36, 16
	v_lshl_add_u64 v[36:37], v[46:47], 0, v[64:65]
	global_load_dwordx4 v[74:77], v[36:37], off offset:16
	global_load_dwordx4 v[78:81], v[36:37], off
	v_cvt_f16_f32_e32 v37, v85
	s_waitcnt vmcnt(12)
	v_cvt_f16_f32_e32 v40, v94
	v_cvt_f16_f32_e32 v44, v93
	v_cvt_pk_f16_f32 v39, v83, v84
	v_alignbit_b32 v36, v39, v38, 16
	v_alignbit_b32 v37, v37, v39, 16
	v_cvt_pk_f16_f32 v39, v95, v96
	v_pack_b32_f16 v38, v40, v39
	v_cvt_pk_f16_f32 v42, v97, v90
	v_cvt_pk_f16_f32 v43, v91, v92
	v_lshl_add_u64 v[40:41], v[46:47], 0, v[66:67]
	v_alignbit_b32 v39, v42, v39, 16
	global_load_dwordx4 v[82:85], v[40:41], off offset:16
	global_load_dwordx4 v[86:89], v[40:41], off
	v_alignbit_b32 v40, v43, v42, 16
	v_alignbit_b32 v41, v44, v43, 16
	v_lshl_add_u64 v[46:47], v[46:47], 0, v[68:69]
	s_mov_b64 s[0:1], 0x4000
	s_waitcnt vmcnt(12)
	v_pk_add_f32 v[42:43], v[102:103], v[102:103]
	v_pk_add_f32 v[44:45], v[104:105], v[104:105]
	v_cvt_pk_f16_f32 v42, v42, v43
	v_cvt_pk_f16_f32 v43, v44, v45
	v_pk_add_f32 v[44:45], v[98:99], v[98:99]
	global_load_dwordx4 v[90:93], v[46:47], off offset:16
	global_load_dwordx4 v[94:97], v[46:47], off
	v_pk_add_f32 v[46:47], v[100:101], v[100:101]
	v_lshl_add_u64 v[120:121], v[58:59], 0, s[0:1]
	v_cvt_pk_f16_f32 v44, v44, v45
	v_cvt_pk_f16_f32 v45, v46, v47
	v_lshl_add_u64 v[50:51], v[120:121], 0, v[62:63]
	global_load_dwordx4 v[98:101], v[50:51], off offset:16
	global_load_dwordx4 v[102:105], v[50:51], off
	v_lshl_add_u64 v[58:59], v[120:121], 0, v[66:67]
	v_or_b32_e32 v60, 0x6000, v72
	s_waitcnt vmcnt(15)
	v_pk_add_f32 v[50:51], v[114:115], v[114:115]
	s_waitcnt vmcnt(14)
	v_pk_add_f32 v[46:47], v[116:117], v[116:117]
	v_pk_add_f32 v[48:49], v[118:119], v[118:119]
	v_cvt_pk_f16_f32 v46, v46, v47
	v_cvt_pk_f16_f32 v47, v48, v49
	v_pk_add_f32 v[48:49], v[112:113], v[112:113]
	s_waitcnt vmcnt(12)
	v_pk_add_f32 v[52:53], v[134:135], v[134:135]
	v_cvt_pk_f16_f32 v48, v48, v49
	v_cvt_pk_f16_f32 v49, v50, v51
	v_pk_add_f32 v[50:51], v[132:133], v[132:133]
	v_pk_add_f32 v[54:55], v[126:127], v[126:127]
	v_cvt_pk_f16_f32 v50, v50, v51
	v_cvt_pk_f16_f32 v51, v52, v53
	v_pk_add_f32 v[52:53], v[124:125], v[124:125]
	v_lshl_add_u64 v[70:71], v[70:71], 0, v[60:61]
	v_cvt_pk_f16_f32 v52, v52, v53
	v_cvt_pk_f16_f32 v53, v54, v55
	v_lshl_add_u64 v[54:55], v[120:121], 0, v[64:65]
	global_load_dwordx4 v[112:115], v[54:55], off offset:16
	global_load_dwordx4 v[116:119], v[54:55], off
	global_load_dwordx4 v[124:127], v[58:59], off offset:16
	global_load_dwordx4 v[132:135], v[58:59], off
	v_lshl_add_u64 v[120:121], v[120:121], 0, v[68:69]
	v_lshl_add_u64 v[60:61], v[70:71], 0, v[62:63]
	s_waitcnt vmcnt(15)
	v_pk_add_f32 v[58:59], v[142:143], v[142:143]
	s_waitcnt vmcnt(14)
	v_pk_add_f32 v[54:55], v[144:145], v[144:145]
	v_pk_add_f32 v[56:57], v[146:147], v[146:147]
	v_cvt_pk_f16_f32 v54, v54, v55
	v_cvt_pk_f16_f32 v55, v56, v57
	v_pk_add_f32 v[56:57], v[140:141], v[140:141]
	global_load_dwordx4 v[140:143], v[120:121], off offset:16
	global_load_dwordx4 v[144:147], v[120:121], off
	v_cvt_pk_f16_f32 v56, v56, v57
	v_cvt_pk_f16_f32 v57, v58, v59
	v_lshl_add_u64 v[64:65], v[70:71], 0, v[64:65]
	s_waitcnt vmcnt(14)
	v_pk_add_f32 v[58:59], v[152:153], v[152:153]
	v_pk_add_f32 v[120:121], v[154:155], v[154:155]
	global_load_dwordx4 v[152:155], v[60:61], off offset:16
	global_load_dwordx4 v[156:159], v[60:61], off
	v_cvt_pk_f16_f32 v58, v58, v59
	v_cvt_pk_f16_f32 v59, v120, v121
	v_pk_add_f32 v[120:121], v[148:149], v[148:149]
	v_pk_add_f32 v[62:63], v[150:151], v[150:151]
	global_load_dwordx4 v[148:151], v[64:65], off offset:16
	global_load_dwordx4 v[160:163], v[64:65], off
	v_lshl_add_u64 v[66:67], v[70:71], 0, v[66:67]
	global_load_dwordx4 v[164:167], v[66:67], off offset:16
	global_load_dwordx4 v[168:171], v[66:67], off
	v_lshl_add_u64 v[68:69], v[70:71], 0, v[68:69]
	global_load_dwordx4 v[172:175], v[68:69], off offset:16
	global_load_dwordx4 v[176:179], v[68:69], off
	v_cvt_pk_f16_f32 v60, v120, v121
	v_cvt_pk_f16_f32 v61, v62, v63
	v_lshlrev_b32_e32 v120, 2, v73
	v_and_b32_e32 v73, 0xcf, v0
	s_waitcnt vmcnt(20)
	v_pk_add_f32 v[62:63], v[78:79], v[78:79]
	v_pk_add_f32 v[64:65], v[80:81], v[80:81]
	v_cvt_pk_f16_f32 v62, v62, v63
	v_cvt_pk_f16_f32 v63, v64, v65
	v_pk_add_f32 v[64:65], v[74:75], v[74:75]
	v_pk_add_f32 v[74:75], v[76:77], v[76:77]
	v_lshlrev_b32_e32 v76, 2, v73
	v_mov_b32_e32 v77, 0xc0
	global_load_dword v110, v120, s[20:21]
	global_load_dword v121, v120, s[20:21] offset:64
	global_load_dword v122, v76, s[8:9]
	v_lshl_or_b32 v77, v0, 2, v77
	global_load_dword v128, v76, s[8:9] offset:64
	global_load_dword v129, v76, s[8:9] offset:128
	global_load_dword v130, v77, s[8:9]
	v_cvt_pk_f16_f32 v64, v64, v65
	v_cvt_pk_f16_f32 v65, v74, v75
	s_waitcnt vmcnt(24)
	v_pk_add_f32 v[66:67], v[86:87], v[86:87]
	v_pk_add_f32 v[74:75], v[88:89], v[88:89]
	v_pk_add_f32 v[68:69], v[82:83], v[82:83]
	v_pk_add_f32 v[70:71], v[84:85], v[84:85]
	v_cvt_pk_f16_f32 v66, v66, v67
	v_cvt_pk_f16_f32 v67, v74, v75
	v_cvt_pk_f16_f32 v68, v68, v69
	v_cvt_pk_f16_f32 v69, v70, v71
	s_movk_i32 s0, 0xc0
	s_waitcnt vmcnt(22)
	v_pk_add_f32 v[70:71], v[94:95], v[94:95]
	v_pk_add_f32 v[74:75], v[96:97], v[96:97]
	v_cvt_pk_f16_f32 v70, v70, v71
	v_cvt_pk_f16_f32 v71, v74, v75
	v_pk_add_f32 v[74:75], v[90:91], v[90:91]
	s_waitcnt vmcnt(21)
	v_pk_add_f32 v[78:79], v[100:101], v[100:101]
	v_cvt_pk_f16_f32 v72, v74, v75
	v_pk_add_f32 v[74:75], v[92:93], v[92:93]
	s_waitcnt vmcnt(20)
	v_pk_add_f32 v[76:77], v[104:105], v[104:105]
	v_cvt_pk_f16_f32 v73, v74, v75
	v_pk_add_f32 v[74:75], v[102:103], v[102:103]
	v_mov_b32_e32 v186, 0
	v_mov_b32_e32 v187, 0
	v_mov_b32_e32 v188, 0
	v_mov_b32_e32 v189, 0
	v_mov_b32_e32 v190, 0x13480
	ds_write_b128 v190, v[186:189]
	s_waitcnt lgkmcnt(0)
	v_cvt_pk_f16_f32 v74, v74, v75
	v_cvt_pk_f16_f32 v75, v76, v77
	v_pk_add_f32 v[76:77], v[98:99], v[98:99]
	s_barrier
	v_cvt_pk_f16_f32 v76, v76, v77
	v_cvt_pk_f16_f32 v77, v78, v79
	s_waitcnt vmcnt(19)
	v_pk_add_f32 v[82:83], v[114:115], v[114:115]
	s_waitcnt vmcnt(18)
	v_pk_add_f32 v[78:79], v[116:117], v[116:117]
	v_pk_add_f32 v[80:81], v[118:119], v[118:119]
	v_cvt_pk_f16_f32 v78, v78, v79
	v_cvt_pk_f16_f32 v79, v80, v81
	v_pk_add_f32 v[80:81], v[112:113], v[112:113]
	s_waitcnt vmcnt(16)
	v_pk_add_f32 v[84:85], v[134:135], v[134:135]
	v_cvt_pk_f16_f32 v80, v80, v81
	v_cvt_pk_f16_f32 v81, v82, v83
	v_pk_add_f32 v[82:83], v[132:133], v[132:133]
	v_pk_add_f32 v[86:87], v[126:127], v[126:127]
	v_cvt_pk_f16_f32 v82, v82, v83
	v_cvt_pk_f16_f32 v83, v84, v85
	v_pk_add_f32 v[84:85], v[124:125], v[124:125]
	s_waitcnt vmcnt(14)
	v_pk_add_f32 v[88:89], v[146:147], v[146:147]
	v_cvt_pk_f16_f32 v84, v84, v85
	v_cvt_pk_f16_f32 v85, v86, v87
	v_pk_add_f32 v[86:87], v[144:145], v[144:145]
	v_pk_add_f32 v[90:91], v[142:143], v[142:143]
	v_cvt_pk_f16_f32 v86, v86, v87
	v_cvt_pk_f16_f32 v87, v88, v89
	v_pk_add_f32 v[88:89], v[140:141], v[140:141]
	s_waitcnt vmcnt(12)
	v_pk_add_f32 v[92:93], v[158:159], v[158:159]
	v_cvt_pk_f16_f32 v88, v88, v89
	v_cvt_pk_f16_f32 v89, v90, v91
	v_pk_add_f32 v[90:91], v[156:157], v[156:157]
	v_pk_add_f32 v[94:95], v[154:155], v[154:155]
	v_cvt_pk_f16_f32 v90, v90, v91
	v_cvt_pk_f16_f32 v91, v92, v93
	v_pk_add_f32 v[92:93], v[152:153], v[152:153]
	s_waitcnt vmcnt(10)
	v_pk_add_f32 v[96:97], v[162:163], v[162:163]
	v_cvt_pk_f16_f32 v92, v92, v93
	v_cvt_pk_f16_f32 v93, v94, v95
	v_pk_add_f32 v[94:95], v[160:161], v[160:161]
	v_pk_add_f32 v[98:99], v[150:151], v[150:151]
	v_cvt_pk_f16_f32 v94, v94, v95
	v_cvt_pk_f16_f32 v95, v96, v97
	v_pk_add_f32 v[96:97], v[148:149], v[148:149]
	s_waitcnt vmcnt(8)
	v_pk_add_f32 v[100:101], v[170:171], v[170:171]
	v_cvt_pk_f16_f32 v96, v96, v97
	v_cvt_pk_f16_f32 v97, v98, v99
	v_pk_add_f32 v[98:99], v[168:169], v[168:169]
	v_pk_add_f32 v[102:103], v[166:167], v[166:167]
	v_cvt_pk_f16_f32 v98, v98, v99
	v_cvt_pk_f16_f32 v99, v100, v101
	v_pk_add_f32 v[100:101], v[164:165], v[164:165]
	s_waitcnt vmcnt(6)
	v_pk_add_f32 v[104:105], v[178:179], v[178:179]
	v_cvt_pk_f16_f32 v100, v100, v101
	v_cvt_pk_f16_f32 v101, v102, v103
	v_pk_add_f32 v[102:103], v[176:177], v[176:177]
	v_lshlrev_b32_e32 v115, 4, v131
	v_cvt_pk_f16_f32 v102, v102, v103
	v_cvt_pk_f16_f32 v103, v104, v105
	v_pk_add_f32 v[104:105], v[172:173], v[172:173]
	v_pk_add_f32 v[112:113], v[174:175], v[174:175]
	v_and_or_b32 v116, v0, s0, v115
	v_cvt_pk_f16_f32 v104, v104, v105
	v_cvt_pk_f16_f32 v105, v112, v113
	v_or_b32_e32 v1, v116, v106
	v_add_u32_e32 v112, 0x129c0, v120
	ds_read2_b32 v[112:113], v112 offset1:16
	v_lshrrev_b32_e32 v117, 3, v1
	v_mov_b32_e32 v1, 0x133c0
	v_lshl_or_b32 v108, v108, 1, v115
	v_lshl_or_b32 v109, v109, 1, v115
	v_lshl_or_b32 v111, v111, 1, v115
	v_add_u32_e32 v148, 0x131c0, v107
	v_add_u32_e32 v149, 0x132c0, v107
	v_mov_b32_e32 v107, 0x13440
	v_lshl_add_u32 v1, v117, 2, v1
	v_add_u32_e32 v139, 0x131c0, v116
	v_add_u32_e32 v140, 0x131c0, v108
	v_add_u32_e32 v141, 0x131c0, v109
	v_add_u32_e32 v142, 0x131c0, v111
	v_add_u32_e32 v143, 0x132c0, v116
	v_add_u32_e32 v144, 0x132c0, v108
	v_add_u32_e32 v145, 0x132c0, v109
	v_add_u32_e32 v146, 0x132c0, v111
	v_or_b32_e32 v147, 0x13440, v115
	v_lshl_or_b32 v150, v117, 1, v107
	v_lshlrev_b32_e32 v151, 2, v123
	ds_read_b32 v152, v1
	ds_read_b32 v153, v151
	s_waitcnt vmcnt(5)
	v_mul_f32_e32 v106, 0x3fb8aa3b, v110
	s_waitcnt vmcnt(4)
	v_mul_f32_e32 v110, 0x3fb8aa3b, v121
	s_waitcnt vmcnt(3)
	v_mul_f32_e32 v114, 0x4038aa3b, v122
	s_waitcnt vmcnt(2)
	v_mul_f32_e32 v118, 0x4038aa3b, v128
	s_waitcnt vmcnt(1)
	v_mul_f32_e32 v122, 0x4038aa3b, v129
	s_waitcnt vmcnt(0)
	v_mul_f32_e32 v126, 0x4038aa3b, v130
	s_waitcnt lgkmcnt(2)
	v_mul_f32_e32 v130, 0x3fb8aa3b, v112
	v_mul_f32_e32 v134, 0x3fb8aa3b, v113
	v_cmp_lt_u32_e64 s[0:1], 1, v131
	v_and_b32_e32 v132, 16, v0
	v_mov_b32_e32 v107, 0
	v_cndmask_b32_e64 v154, v130, v134, s[0:1]
	v_mov_b32_e32 v108, 0
	v_mov_b32_e32 v109, 0
	v_mov_b32_e32 v111, 0
	v_mov_b32_e32 v112, 0
	v_mov_b32_e32 v113, 0
	v_mov_b32_e32 v115, 0
	v_mov_b32_e32 v116, 0
	v_mov_b32_e32 v117, 0
	v_mov_b32_e32 v119, 0
	v_mov_b32_e32 v120, 0
	v_mov_b32_e32 v121, 0
	v_mov_b32_e32 v123, 0
	v_mov_b32_e32 v124, 0
	v_mov_b32_e32 v125, 0
	v_mov_b32_e32 v127, 0
	v_mov_b32_e32 v128, 0
	v_mov_b32_e32 v129, 0
	v_cmp_eq_u32_e64 s[6:7], 0, v132
	v_mov_b32_e32 v135, 0
	v_mov_b32_e32 v136, 0
	v_mov_b32_e32 v137, 0
	v_mov_b32_e32 v131, 0
	v_mov_b32_e32 v132, 0
	v_mov_b32_e32 v133, 0
	v_and_b32_e32 v187, 2, v0
	v_and_b32_e32 v188, 1, v0
	v_cmp_ne_u32_e64 s[46:47], 0, v187
	v_cmp_ne_u32_e64 s[48:49], 0, v188
	v_mov_b32_e32 v189, 0x44444444
	v_mov_b32_e32 v191, 0xeeeeeeee
	v_cndmask_b32_e64 v191, v189, v191, s[48:49]
	v_cndmask_b32_e64 v139, v139, v190, s[46:47]
	v_cndmask_b32_e64 v140, v140, v190, s[46:47]
	v_cndmask_b32_e64 v141, v141, v190, s[46:47]
	v_cndmask_b32_e64 v142, v142, v190, s[46:47]
	v_cndmask_b32_e64 v143, v143, v190, s[46:47]
	v_cndmask_b32_e64 v144, v144, v190, s[46:47]
	v_cndmask_b32_e64 v145, v145, v190, s[46:47]
	v_cndmask_b32_e64 v146, v146, v190, s[46:47]
	v_cndmask_b32_e64 v147, v147, v190, s[46:47]
	v_mov_b32_e32 v192, 0
	v_mov_b32_e32 v193, 0
	v_mov_b32_e32 v194, 0
	v_mov_b32_e32 v195, 0
	v_mov_b32_e32 v196, 0
	v_mov_b32_e32 v197, 0
	v_mov_b32_e32 v198, 0
	v_mov_b32_e32 v199, 0
	v_mov_b32_e32 v200, 0
	v_mov_b32_e32 v201, 0
	v_mov_b32_e32 v202, 0
	v_mov_b32_e32 v203, 0
	v_mov_b32_e32 v204, 0
	v_mov_b32_e32 v205, 0
	v_mov_b32_e32 v206, 0
	v_mov_b32_e32 v207, 0
	v_and_b32_e32 v240, 15, v0
	v_bfe_u32 v241, v0, 5, 1
	v_lshl_add_u32 v242, v241, 4, v240
	v_lshlrev_b32_e32 v242, 2, v242
	v_add_u32_e32 v243, 128, v242
	v_and_b32_e32 v241, 16, v0
	v_cmp_ne_u32_e64 s[50:51], 0, v241
	ds_bpermute_b32 v244, v242, v6
	ds_bpermute_b32 v245, v242, v8
	s_waitcnt lgkmcnt(0)
	v_cndmask_b32_e64 v208, v244, v245, s[50:51]
	ds_bpermute_b32 v244, v242, v26
	ds_bpermute_b32 v245, v242, v28
	s_waitcnt lgkmcnt(0)
	v_cndmask_b32_e64 v209, v244, v245, s[50:51]
	ds_bpermute_b32 v244, v242, v7
	ds_bpermute_b32 v245, v242, v9
	s_waitcnt lgkmcnt(0)
	v_cndmask_b32_e64 v210, v244, v245, s[50:51]
	ds_bpermute_b32 v244, v242, v27
	ds_bpermute_b32 v245, v242, v29
	s_waitcnt lgkmcnt(0)
	v_cndmask_b32_e64 v211, v244, v245, s[50:51]
	ds_bpermute_b32 v244, v243, v6
	ds_bpermute_b32 v245, v243, v8
	s_waitcnt lgkmcnt(0)
	v_cndmask_b32_e64 v212, v244, v245, s[50:51]
	ds_bpermute_b32 v244, v243, v26
	ds_bpermute_b32 v245, v243, v28
	s_waitcnt lgkmcnt(0)
	v_cndmask_b32_e64 v213, v244, v245, s[50:51]
	ds_bpermute_b32 v244, v243, v7
	ds_bpermute_b32 v245, v243, v9
	s_waitcnt lgkmcnt(0)
	v_cndmask_b32_e64 v214, v244, v245, s[50:51]
	ds_bpermute_b32 v244, v243, v27
	ds_bpermute_b32 v245, v243, v29
	s_waitcnt lgkmcnt(0)
	v_cndmask_b32_e64 v215, v244, v245, s[50:51]
	ds_bpermute_b32 v244, v242, v10
	ds_bpermute_b32 v245, v242, v12
	s_waitcnt lgkmcnt(0)
	v_cndmask_b32_e64 v216, v244, v245, s[50:51]
	ds_bpermute_b32 v244, v242, v30
	ds_bpermute_b32 v245, v242, v32
	s_waitcnt lgkmcnt(0)
	v_cndmask_b32_e64 v217, v244, v245, s[50:51]
	ds_bpermute_b32 v244, v242, v11
	ds_bpermute_b32 v245, v242, v13
	s_waitcnt lgkmcnt(0)
	v_cndmask_b32_e64 v218, v244, v245, s[50:51]
	ds_bpermute_b32 v244, v242, v31
	ds_bpermute_b32 v245, v242, v33
	s_waitcnt lgkmcnt(0)
	v_cndmask_b32_e64 v219, v244, v245, s[50:51]
	ds_bpermute_b32 v244, v243, v10
	ds_bpermute_b32 v245, v243, v12
	s_waitcnt lgkmcnt(0)
	v_cndmask_b32_e64 v220, v244, v245, s[50:51]
	ds_bpermute_b32 v244, v243, v30
	ds_bpermute_b32 v245, v243, v32
	s_waitcnt lgkmcnt(0)
	v_cndmask_b32_e64 v221, v244, v245, s[50:51]
	ds_bpermute_b32 v244, v243, v11
	ds_bpermute_b32 v245, v243, v13
	s_waitcnt lgkmcnt(0)
	v_cndmask_b32_e64 v222, v244, v245, s[50:51]
	ds_bpermute_b32 v244, v243, v31
	ds_bpermute_b32 v245, v243, v33
	s_waitcnt lgkmcnt(0)
	v_cndmask_b32_e64 v223, v244, v245, s[50:51]
	ds_bpermute_b32 v244, v242, v14
	ds_bpermute_b32 v245, v242, v16
	s_waitcnt lgkmcnt(0)
	v_cndmask_b32_e64 v224, v244, v245, s[50:51]
	ds_bpermute_b32 v244, v242, v34
	ds_bpermute_b32 v245, v242, v36
	s_waitcnt lgkmcnt(0)
	v_cndmask_b32_e64 v225, v244, v245, s[50:51]
	ds_bpermute_b32 v244, v242, v15
	ds_bpermute_b32 v245, v242, v17
	s_waitcnt lgkmcnt(0)
	v_cndmask_b32_e64 v226, v244, v245, s[50:51]
	ds_bpermute_b32 v244, v242, v35
	ds_bpermute_b32 v245, v242, v37
	s_waitcnt lgkmcnt(0)
	v_cndmask_b32_e64 v227, v244, v245, s[50:51]
	ds_bpermute_b32 v244, v243, v14
	ds_bpermute_b32 v245, v243, v16
	s_waitcnt lgkmcnt(0)
	v_cndmask_b32_e64 v228, v244, v245, s[50:51]
	ds_bpermute_b32 v244, v243, v34
	ds_bpermute_b32 v245, v243, v36
	s_waitcnt lgkmcnt(0)
	v_cndmask_b32_e64 v229, v244, v245, s[50:51]
	ds_bpermute_b32 v244, v243, v15
	ds_bpermute_b32 v245, v243, v17
	s_waitcnt lgkmcnt(0)
	v_cndmask_b32_e64 v230, v244, v245, s[50:51]
	ds_bpermute_b32 v244, v243, v35
	ds_bpermute_b32 v245, v243, v37
	s_waitcnt lgkmcnt(0)
	v_cndmask_b32_e64 v231, v244, v245, s[50:51]
	ds_bpermute_b32 v244, v242, v18
	ds_bpermute_b32 v245, v242, v20
	s_waitcnt lgkmcnt(0)
	v_cndmask_b32_e64 v232, v244, v245, s[50:51]
	ds_bpermute_b32 v244, v242, v38
	ds_bpermute_b32 v245, v242, v40
	s_waitcnt lgkmcnt(0)
	v_cndmask_b32_e64 v233, v244, v245, s[50:51]
	ds_bpermute_b32 v244, v242, v19
	ds_bpermute_b32 v245, v242, v21
	s_waitcnt lgkmcnt(0)
	v_cndmask_b32_e64 v234, v244, v245, s[50:51]
	ds_bpermute_b32 v244, v242, v39
	ds_bpermute_b32 v245, v242, v41
	s_waitcnt lgkmcnt(0)
	v_cndmask_b32_e64 v235, v244, v245, s[50:51]
	ds_bpermute_b32 v244, v243, v18
	ds_bpermute_b32 v245, v243, v20
	s_waitcnt lgkmcnt(0)
	v_cndmask_b32_e64 v236, v244, v245, s[50:51]
	ds_bpermute_b32 v244, v243, v38
	ds_bpermute_b32 v245, v243, v40
	s_waitcnt lgkmcnt(0)
	v_cndmask_b32_e64 v237, v244, v245, s[50:51]
	ds_bpermute_b32 v244, v243, v19
	ds_bpermute_b32 v245, v243, v21
	s_waitcnt lgkmcnt(0)
	v_cndmask_b32_e64 v238, v244, v245, s[50:51]
	ds_bpermute_b32 v244, v243, v39
	ds_bpermute_b32 v245, v243, v41
	s_waitcnt lgkmcnt(0)
	v_cndmask_b32_e64 v239, v244, v245, s[50:51]
	v_mov_b32_e32 v6, v208
	v_mov_b32_e32 v7, v209
	v_mov_b32_e32 v8, v210
	v_mov_b32_e32 v9, v211
	v_mov_b32_e32 v10, v212
	v_mov_b32_e32 v11, v213
	v_mov_b32_e32 v12, v214
	v_mov_b32_e32 v13, v215
	v_mov_b32_e32 v14, v216
	v_mov_b32_e32 v15, v217
	v_mov_b32_e32 v16, v218
	v_mov_b32_e32 v17, v219
	v_mov_b32_e32 v18, v220
	v_mov_b32_e32 v19, v221
	v_mov_b32_e32 v20, v222
	v_mov_b32_e32 v21, v223
	v_mov_b32_e32 v26, v224
	v_mov_b32_e32 v27, v225
	v_mov_b32_e32 v28, v226
	v_mov_b32_e32 v29, v227
	v_mov_b32_e32 v30, v228
	v_mov_b32_e32 v31, v229
	v_mov_b32_e32 v32, v230
	v_mov_b32_e32 v33, v231
	v_mov_b32_e32 v34, v232
	v_mov_b32_e32 v35, v233
	v_mov_b32_e32 v36, v234
	v_mov_b32_e32 v37, v235
	v_mov_b32_e32 v38, v236
	v_mov_b32_e32 v39, v237
	v_mov_b32_e32 v40, v238
	v_mov_b32_e32 v41, v239
	ds_bpermute_b32 v244, v242, v42
	ds_bpermute_b32 v245, v242, v44
	s_waitcnt lgkmcnt(0)
	v_cndmask_b32_e64 v208, v244, v245, s[50:51]
	ds_bpermute_b32 v244, v242, v58
	ds_bpermute_b32 v245, v242, v60
	s_waitcnt lgkmcnt(0)
	v_cndmask_b32_e64 v209, v244, v245, s[50:51]
	ds_bpermute_b32 v244, v242, v43
	ds_bpermute_b32 v245, v242, v45
	s_waitcnt lgkmcnt(0)
	v_cndmask_b32_e64 v210, v244, v245, s[50:51]
	ds_bpermute_b32 v244, v242, v59
	ds_bpermute_b32 v245, v242, v61
	s_waitcnt lgkmcnt(0)
	v_cndmask_b32_e64 v211, v244, v245, s[50:51]
	ds_bpermute_b32 v244, v243, v42
	ds_bpermute_b32 v245, v243, v44
	s_waitcnt lgkmcnt(0)
	v_cndmask_b32_e64 v212, v244, v245, s[50:51]
	ds_bpermute_b32 v244, v243, v58
	ds_bpermute_b32 v245, v243, v60
	s_waitcnt lgkmcnt(0)
	v_cndmask_b32_e64 v213, v244, v245, s[50:51]
	ds_bpermute_b32 v244, v243, v43
	ds_bpermute_b32 v245, v243, v45
	s_waitcnt lgkmcnt(0)
	v_cndmask_b32_e64 v214, v244, v245, s[50:51]
	ds_bpermute_b32 v244, v243, v59
	ds_bpermute_b32 v245, v243, v61
	s_waitcnt lgkmcnt(0)
	v_cndmask_b32_e64 v215, v244, v245, s[50:51]
	ds_bpermute_b32 v244, v242, v46
	ds_bpermute_b32 v245, v242, v48
	s_waitcnt lgkmcnt(0)
	v_cndmask_b32_e64 v216, v244, v245, s[50:51]
	ds_bpermute_b32 v244, v242, v62
	ds_bpermute_b32 v245, v242, v64
	s_waitcnt lgkmcnt(0)
	v_cndmask_b32_e64 v217, v244, v245, s[50:51]
	ds_bpermute_b32 v244, v242, v47
	ds_bpermute_b32 v245, v242, v49
	s_waitcnt lgkmcnt(0)
	v_cndmask_b32_e64 v218, v244, v245, s[50:51]
	ds_bpermute_b32 v244, v242, v63
	ds_bpermute_b32 v245, v242, v65
	s_waitcnt lgkmcnt(0)
	v_cndmask_b32_e64 v219, v244, v245, s[50:51]
	ds_bpermute_b32 v244, v243, v46
	ds_bpermute_b32 v245, v243, v48
	s_waitcnt lgkmcnt(0)
	v_cndmask_b32_e64 v220, v244, v245, s[50:51]
	ds_bpermute_b32 v244, v243, v62
	ds_bpermute_b32 v245, v243, v64
	s_waitcnt lgkmcnt(0)
	v_cndmask_b32_e64 v221, v244, v245, s[50:51]
	ds_bpermute_b32 v244, v243, v47
	ds_bpermute_b32 v245, v243, v49
	s_waitcnt lgkmcnt(0)
	v_cndmask_b32_e64 v222, v244, v245, s[50:51]
	ds_bpermute_b32 v244, v243, v63
	ds_bpermute_b32 v245, v243, v65
	s_waitcnt lgkmcnt(0)
	v_cndmask_b32_e64 v223, v244, v245, s[50:51]
	ds_bpermute_b32 v244, v242, v50
	ds_bpermute_b32 v245, v242, v52
	s_waitcnt lgkmcnt(0)
	v_cndmask_b32_e64 v224, v244, v245, s[50:51]
	ds_bpermute_b32 v244, v242, v66
	ds_bpermute_b32 v245, v242, v68
	s_waitcnt lgkmcnt(0)
	v_cndmask_b32_e64 v225, v244, v245, s[50:51]
	ds_bpermute_b32 v244, v242, v51
	ds_bpermute_b32 v245, v242, v53
	s_waitcnt lgkmcnt(0)
	v_cndmask_b32_e64 v226, v244, v245, s[50:51]
	ds_bpermute_b32 v244, v242, v67
	ds_bpermute_b32 v245, v242, v69
	s_waitcnt lgkmcnt(0)
	v_cndmask_b32_e64 v227, v244, v245, s[50:51]
	ds_bpermute_b32 v244, v243, v50
	ds_bpermute_b32 v245, v243, v52
	s_waitcnt lgkmcnt(0)
	v_cndmask_b32_e64 v228, v244, v245, s[50:51]
	ds_bpermute_b32 v244, v243, v66
	ds_bpermute_b32 v245, v243, v68
	s_waitcnt lgkmcnt(0)
	v_cndmask_b32_e64 v229, v244, v245, s[50:51]
	ds_bpermute_b32 v244, v243, v51
	ds_bpermute_b32 v245, v243, v53
	s_waitcnt lgkmcnt(0)
	v_cndmask_b32_e64 v230, v244, v245, s[50:51]
	ds_bpermute_b32 v244, v243, v67
	ds_bpermute_b32 v245, v243, v69
	s_waitcnt lgkmcnt(0)
	v_cndmask_b32_e64 v231, v244, v245, s[50:51]
	ds_bpermute_b32 v244, v242, v54
	ds_bpermute_b32 v245, v242, v56
	s_waitcnt lgkmcnt(0)
	v_cndmask_b32_e64 v232, v244, v245, s[50:51]
	ds_bpermute_b32 v244, v242, v70
	ds_bpermute_b32 v245, v242, v72
	s_waitcnt lgkmcnt(0)
	v_cndmask_b32_e64 v233, v244, v245, s[50:51]
	ds_bpermute_b32 v244, v242, v55
	ds_bpermute_b32 v245, v242, v57
	s_waitcnt lgkmcnt(0)
	v_cndmask_b32_e64 v234, v244, v245, s[50:51]
	ds_bpermute_b32 v244, v242, v71
	ds_bpermute_b32 v245, v242, v73
	s_waitcnt lgkmcnt(0)
	v_cndmask_b32_e64 v235, v244, v245, s[50:51]
	ds_bpermute_b32 v244, v243, v54
	ds_bpermute_b32 v245, v243, v56
	s_waitcnt lgkmcnt(0)
	v_cndmask_b32_e64 v236, v244, v245, s[50:51]
	ds_bpermute_b32 v244, v243, v70
	ds_bpermute_b32 v245, v243, v72
	s_waitcnt lgkmcnt(0)
	v_cndmask_b32_e64 v237, v244, v245, s[50:51]
	ds_bpermute_b32 v244, v243, v55
	ds_bpermute_b32 v245, v243, v57
	s_waitcnt lgkmcnt(0)
	v_cndmask_b32_e64 v238, v244, v245, s[50:51]
	ds_bpermute_b32 v244, v243, v71
	ds_bpermute_b32 v245, v243, v73
	s_waitcnt lgkmcnt(0)
	v_cndmask_b32_e64 v239, v244, v245, s[50:51]
	v_mov_b32_e32 v42, v208
	v_mov_b32_e32 v43, v209
	v_mov_b32_e32 v44, v210
	v_mov_b32_e32 v45, v211
	v_mov_b32_e32 v46, v212
	v_mov_b32_e32 v47, v213
	v_mov_b32_e32 v48, v214
	v_mov_b32_e32 v49, v215
	v_mov_b32_e32 v50, v216
	v_mov_b32_e32 v51, v217
	v_mov_b32_e32 v52, v218
	v_mov_b32_e32 v53, v219
	v_mov_b32_e32 v54, v220
	v_mov_b32_e32 v55, v221
	v_mov_b32_e32 v56, v222
	v_mov_b32_e32 v57, v223
	v_mov_b32_e32 v58, v224
	v_mov_b32_e32 v59, v225
	v_mov_b32_e32 v60, v226
	v_mov_b32_e32 v61, v227
	v_mov_b32_e32 v62, v228
	v_mov_b32_e32 v63, v229
	v_mov_b32_e32 v64, v230
	v_mov_b32_e32 v65, v231
	v_mov_b32_e32 v66, v232
	v_mov_b32_e32 v67, v233
	v_mov_b32_e32 v68, v234
	v_mov_b32_e32 v69, v235
	v_mov_b32_e32 v70, v236
	v_mov_b32_e32 v71, v237
	v_mov_b32_e32 v72, v238
	v_mov_b32_e32 v73, v239
	ds_bpermute_b32 v244, v242, v74
	ds_bpermute_b32 v245, v242, v76
	s_waitcnt lgkmcnt(0)
	v_cndmask_b32_e64 v208, v244, v245, s[50:51]
	ds_bpermute_b32 v244, v242, v90
	ds_bpermute_b32 v245, v242, v92
	s_waitcnt lgkmcnt(0)
	v_cndmask_b32_e64 v209, v244, v245, s[50:51]
	ds_bpermute_b32 v244, v242, v75
	ds_bpermute_b32 v245, v242, v77
	s_waitcnt lgkmcnt(0)
	v_cndmask_b32_e64 v210, v244, v245, s[50:51]
	ds_bpermute_b32 v244, v242, v91
	ds_bpermute_b32 v245, v242, v93
	s_waitcnt lgkmcnt(0)
	v_cndmask_b32_e64 v211, v244, v245, s[50:51]
	ds_bpermute_b32 v244, v243, v74
	ds_bpermute_b32 v245, v243, v76
	s_waitcnt lgkmcnt(0)
	v_cndmask_b32_e64 v212, v244, v245, s[50:51]
	ds_bpermute_b32 v244, v243, v90
	ds_bpermute_b32 v245, v243, v92
	s_waitcnt lgkmcnt(0)
	v_cndmask_b32_e64 v213, v244, v245, s[50:51]
	ds_bpermute_b32 v244, v243, v75
	ds_bpermute_b32 v245, v243, v77
	s_waitcnt lgkmcnt(0)
	v_cndmask_b32_e64 v214, v244, v245, s[50:51]
	ds_bpermute_b32 v244, v243, v91
	ds_bpermute_b32 v245, v243, v93
	s_waitcnt lgkmcnt(0)
	v_cndmask_b32_e64 v215, v244, v245, s[50:51]
	ds_bpermute_b32 v244, v242, v78
	ds_bpermute_b32 v245, v242, v80
	s_waitcnt lgkmcnt(0)
	v_cndmask_b32_e64 v216, v244, v245, s[50:51]
	ds_bpermute_b32 v244, v242, v94
	ds_bpermute_b32 v245, v242, v96
	s_waitcnt lgkmcnt(0)
	v_cndmask_b32_e64 v217, v244, v245, s[50:51]
	ds_bpermute_b32 v244, v242, v79
	ds_bpermute_b32 v245, v242, v81
	s_waitcnt lgkmcnt(0)
	v_cndmask_b32_e64 v218, v244, v245, s[50:51]
	ds_bpermute_b32 v244, v242, v95
	ds_bpermute_b32 v245, v242, v97
	s_waitcnt lgkmcnt(0)
	v_cndmask_b32_e64 v219, v244, v245, s[50:51]
	ds_bpermute_b32 v244, v243, v78
	ds_bpermute_b32 v245, v243, v80
	s_waitcnt lgkmcnt(0)
	v_cndmask_b32_e64 v220, v244, v245, s[50:51]
	ds_bpermute_b32 v244, v243, v94
	ds_bpermute_b32 v245, v243, v96
	s_waitcnt lgkmcnt(0)
	v_cndmask_b32_e64 v221, v244, v245, s[50:51]
	ds_bpermute_b32 v244, v243, v79
	ds_bpermute_b32 v245, v243, v81
	s_waitcnt lgkmcnt(0)
	v_cndmask_b32_e64 v222, v244, v245, s[50:51]
	ds_bpermute_b32 v244, v243, v95
	ds_bpermute_b32 v245, v243, v97
	s_waitcnt lgkmcnt(0)
	v_cndmask_b32_e64 v223, v244, v245, s[50:51]
	ds_bpermute_b32 v244, v242, v82
	ds_bpermute_b32 v245, v242, v84
	s_waitcnt lgkmcnt(0)
	v_cndmask_b32_e64 v224, v244, v245, s[50:51]
	ds_bpermute_b32 v244, v242, v98
	ds_bpermute_b32 v245, v242, v100
	s_waitcnt lgkmcnt(0)
	v_cndmask_b32_e64 v225, v244, v245, s[50:51]
	ds_bpermute_b32 v244, v242, v83
	ds_bpermute_b32 v245, v242, v85
	s_waitcnt lgkmcnt(0)
	v_cndmask_b32_e64 v226, v244, v245, s[50:51]
	ds_bpermute_b32 v244, v242, v99
	ds_bpermute_b32 v245, v242, v101
	s_waitcnt lgkmcnt(0)
	v_cndmask_b32_e64 v227, v244, v245, s[50:51]
	ds_bpermute_b32 v244, v243, v82
	ds_bpermute_b32 v245, v243, v84
	s_waitcnt lgkmcnt(0)
	v_cndmask_b32_e64 v228, v244, v245, s[50:51]
	ds_bpermute_b32 v244, v243, v98
	ds_bpermute_b32 v245, v243, v100
	s_waitcnt lgkmcnt(0)
	v_cndmask_b32_e64 v229, v244, v245, s[50:51]
	ds_bpermute_b32 v244, v243, v83
	ds_bpermute_b32 v245, v243, v85
	s_waitcnt lgkmcnt(0)
	v_cndmask_b32_e64 v230, v244, v245, s[50:51]
	ds_bpermute_b32 v244, v243, v99
	ds_bpermute_b32 v245, v243, v101
	s_waitcnt lgkmcnt(0)
	v_cndmask_b32_e64 v231, v244, v245, s[50:51]
	ds_bpermute_b32 v244, v242, v86
	ds_bpermute_b32 v245, v242, v88
	s_waitcnt lgkmcnt(0)
	v_cndmask_b32_e64 v232, v244, v245, s[50:51]
	ds_bpermute_b32 v244, v242, v102
	ds_bpermute_b32 v245, v242, v104
	s_waitcnt lgkmcnt(0)
	v_cndmask_b32_e64 v233, v244, v245, s[50:51]
	ds_bpermute_b32 v244, v242, v87
	ds_bpermute_b32 v245, v242, v89
	s_waitcnt lgkmcnt(0)
	v_cndmask_b32_e64 v234, v244, v245, s[50:51]
	ds_bpermute_b32 v244, v242, v103
	ds_bpermute_b32 v245, v242, v105
	s_waitcnt lgkmcnt(0)
	v_cndmask_b32_e64 v235, v244, v245, s[50:51]
	ds_bpermute_b32 v244, v243, v86
	ds_bpermute_b32 v245, v243, v88
	s_waitcnt lgkmcnt(0)
	v_cndmask_b32_e64 v236, v244, v245, s[50:51]
	ds_bpermute_b32 v244, v243, v102
	ds_bpermute_b32 v245, v243, v104
	s_waitcnt lgkmcnt(0)
	v_cndmask_b32_e64 v237, v244, v245, s[50:51]
	ds_bpermute_b32 v244, v243, v87
	ds_bpermute_b32 v245, v243, v89
	s_waitcnt lgkmcnt(0)
	v_cndmask_b32_e64 v238, v244, v245, s[50:51]
	ds_bpermute_b32 v244, v243, v103
	ds_bpermute_b32 v245, v243, v105
	s_waitcnt lgkmcnt(0)
	v_cndmask_b32_e64 v239, v244, v245, s[50:51]
	v_mov_b32_e32 v74, v208
	v_mov_b32_e32 v75, v209
	v_mov_b32_e32 v76, v210
	v_mov_b32_e32 v77, v211
	v_mov_b32_e32 v78, v212
	v_mov_b32_e32 v79, v213
	v_mov_b32_e32 v80, v214
	v_mov_b32_e32 v81, v215
	v_mov_b32_e32 v82, v216
	v_mov_b32_e32 v83, v217
	v_mov_b32_e32 v84, v218
	v_mov_b32_e32 v85, v219
	v_mov_b32_e32 v86, v220
	v_mov_b32_e32 v87, v221
	v_mov_b32_e32 v88, v222
	v_mov_b32_e32 v89, v223
	v_mov_b32_e32 v90, v224
	v_mov_b32_e32 v91, v225
	v_mov_b32_e32 v92, v226
	v_mov_b32_e32 v93, v227
	v_mov_b32_e32 v94, v228
	v_mov_b32_e32 v95, v229
	v_mov_b32_e32 v96, v230
	v_mov_b32_e32 v97, v231
	v_mov_b32_e32 v98, v232
	v_mov_b32_e32 v99, v233
	v_mov_b32_e32 v100, v234
	v_mov_b32_e32 v101, v235
	v_mov_b32_e32 v102, v236
	v_mov_b32_e32 v103, v237
	v_mov_b32_e32 v104, v238
	v_mov_b32_e32 v105, v239
	ds_bpermute_b32 v244, v242, v2
	ds_bpermute_b32 v245, v242, v4
	s_waitcnt lgkmcnt(0)
	v_cndmask_b32_e64 v248, v244, v245, s[50:51]
	ds_bpermute_b32 v244, v242, v22
	ds_bpermute_b32 v245, v242, v24
	s_waitcnt lgkmcnt(0)
	v_cndmask_b32_e64 v249, v244, v245, s[50:51]
	ds_bpermute_b32 v244, v242, v3
	ds_bpermute_b32 v245, v242, v5
	s_waitcnt lgkmcnt(0)
	v_cndmask_b32_e64 v250, v244, v245, s[50:51]
	ds_bpermute_b32 v244, v242, v23
	ds_bpermute_b32 v245, v242, v25
	s_waitcnt lgkmcnt(0)
	v_cndmask_b32_e64 v251, v244, v245, s[50:51]
	ds_bpermute_b32 v244, v243, v2
	ds_bpermute_b32 v245, v243, v4
	s_waitcnt lgkmcnt(0)
	v_cndmask_b32_e64 v252, v244, v245, s[50:51]
	ds_bpermute_b32 v244, v243, v22
	ds_bpermute_b32 v245, v243, v24
	s_waitcnt lgkmcnt(0)
	v_cndmask_b32_e64 v253, v244, v245, s[50:51]
	ds_bpermute_b32 v244, v243, v3
	ds_bpermute_b32 v245, v243, v5
	s_waitcnt lgkmcnt(0)
	v_cndmask_b32_e64 v254, v244, v245, s[50:51]
	ds_bpermute_b32 v244, v243, v23
	ds_bpermute_b32 v245, v243, v25
	s_waitcnt lgkmcnt(0)
	v_cndmask_b32_e64 v255, v244, v245, s[50:51]
	v_mov_b32_e32 v131, v134
	.p2align 6
.LBB0_21:
	v_exp_f32_e64 v156, -|v154|
	v_max_f32 v157, 0, v154
	v_add_f32 v156, 1.0, v156
	v_log_f32 v156, v156
	s_nop 0
	v_fma_mixlo_f16 v155, v156, 1.0, v157
	ds_write_b16 v148, v155
	v_mov_b32_e32 v192, v106
	v_mov_b32_e32 v193, v110
	v_mul_f32 v182, -2.0, v153
	ds_read_b128 v[208:211], v139
	s_waitcnt lgkmcnt(1)
	s_barrier
	ds_read_b128 v[212:215], v140
	s_waitcnt lgkmcnt(1)
	v_smfmac_f32_16x16x64_f16 v[192:195], v[208:211], v[6:13], v191
	ds_read_b128 v[216:219], v141
	s_waitcnt lgkmcnt(1)
	v_smfmac_f32_16x16x64_f16 v[192:195], v[212:215], v[14:21], v191
	ds_read_b128 v[220:223], v142
	s_waitcnt lgkmcnt(1)
	v_smfmac_f32_16x16x64_f16 v[192:195], v[216:219], v[26:33], v191
	s_waitcnt lgkmcnt(0)
	v_smfmac_f32_16x16x64_f16 v[192:195], v[220:223], v[34:41], v191
	s_nop 7
	v_cndmask_b32_e64 v154, v192, v193, s[0:1]
	v_exp_f32_e64 v156, -|v154|
	v_max_f32 v157, 0, v154
	v_add_f32 v156, 1.0, v156
	v_log_f32 v156, v156
	s_nop 0
	v_fma_mixlo_f16 v155, v156, 1.0, v157
	ds_write_b16 v149, v155
	v_mov_b32_e32 v200, v114
	v_mov_b32_e32 v201, v118
	v_mov_b32_e32 v204, v122
	v_mov_b32_e32 v205, v126
	ds_read_b128 v[208:211], v143
	s_waitcnt lgkmcnt(1)
	s_barrier
	ds_read_b128 v[212:215], v144
	s_waitcnt lgkmcnt(1)
	v_smfmac_f32_16x16x64_f16 v[200:203], v[208:211], v[42:49], v191
	ds_read_b128 v[216:219], v145
	v_smfmac_f32_16x16x64_f16 v[204:207], v[208:211], v[74:81], v191
	ds_read_b128 v[220:223], v146
	s_waitcnt lgkmcnt(2)
	v_smfmac_f32_16x16x64_f16 v[200:203], v[212:215], v[50:57], v191
	v_smfmac_f32_16x16x64_f16 v[204:207], v[212:215], v[82:89], v191
	s_waitcnt lgkmcnt(1)
	v_smfmac_f32_16x16x64_f16 v[200:203], v[216:219], v[58:65], v191
	v_smfmac_f32_16x16x64_f16 v[204:207], v[216:219], v[90:97], v191
	s_waitcnt lgkmcnt(0)
	v_smfmac_f32_16x16x64_f16 v[200:203], v[220:223], v[66:73], v191
	v_smfmac_f32_16x16x64_f16 v[204:207], v[220:223], v[98:105], v191
	s_nop 6
	v_cndmask_b32_e64 v170, v201, v200, s[6:7]
	v_cndmask_b32_e64 v170, v170, v204, s[0:1]
	v_cndmask_b32_e64 v170, v170, v205, s[4:5]
	v_exp_f32_e32 v170, v170
	s_nop 0
	v_add_f32_e32 v170, 1.0, v170
	v_rcp_f32_e32 v170, v170
	s_nop 0
	v_fmac_f32_e32 v153, v170, v182
	s_nop 1
	v_add_f32_dpp v153, v153, v153 quad_perm:[1,0,3,2] row_mask:0xf bank_mask:0xf bound_ctrl:1
	s_nop 1
	v_add_f32_dpp v153, v153, v153 quad_perm:[2,3,0,1] row_mask:0xf bank_mask:0xf bound_ctrl:1
	s_nop 1
	v_add_f32_dpp v153, v153, v153 row_half_mirror row_mask:0xf bank_mask:0xf bound_ctrl:1
	v_cvt_f16_f32_e32 v170, v153
	ds_write_b16 v150, v170
	s_waitcnt lgkmcnt(0)
	s_barrier
	ds_read_b128 v[154:157], v147
	s_waitcnt lgkmcnt(0)
	v_smfmac_f32_16x16x64_f16 v[130:133], v[154:157], v[248:255], v191
	s_nop 2
	v_add_u32_e32 v134, s3, v151
	ds_read_b32 v135, v134
	s_nop 2
	v_cndmask_b32_e64 v136, v130, v131, s[0:1]
	v_exp_f32_e64 v158, -|v136|
	v_max_f32 v159, 0, v136
	v_add_f32 v158, 1.0, v158
	v_log_f32 v158, v158
	s_nop 0
	v_fma_mixlo_f16 v137, v158, 1.0, v159
	ds_write_b16 v148, v137
	v_mov_b32_e32 v192, v106
	v_mov_b32_e32 v193, v110
	v_add_f32_e32 v136, v152, v153
	v_mul_f32 v137, -2.0, v135
	ds_read_b128 v[208:211], v139
	s_waitcnt lgkmcnt(1)
	s_barrier
	ds_read_b128 v[212:215], v140
	s_waitcnt lgkmcnt(1)
	v_smfmac_f32_16x16x64_f16 v[192:195], v[208:211], v[6:13], v191
	ds_read_b128 v[216:219], v141
	s_waitcnt lgkmcnt(1)
	v_smfmac_f32_16x16x64_f16 v[192:195], v[212:215], v[14:21], v191
	ds_read_b128 v[220:223], v142
	s_waitcnt lgkmcnt(1)
	v_smfmac_f32_16x16x64_f16 v[192:195], v[216:219], v[26:33], v191
	s_waitcnt lgkmcnt(0)
	v_smfmac_f32_16x16x64_f16 v[192:195], v[220:223], v[34:41], v191
	s_nop 7
	v_cndmask_b32_e64 v152, v192, v193, s[0:1]
	v_exp_f32_e64 v158, -|v152|
	v_max_f32 v159, 0, v152
	v_add_f32 v158, 1.0, v158
	v_log_f32 v158, v158
	s_nop 0
	v_fma_mixlo_f16 v153, v158, 1.0, v159
	ds_write_b16 v149, v153
	v_mov_b32_e32 v200, v114
	v_mov_b32_e32 v201, v118
	v_mov_b32_e32 v204, v122
	v_mov_b32_e32 v205, v126
	ds_read_b128 v[208:211], v143
	s_waitcnt lgkmcnt(1)
	s_barrier
	ds_read_b128 v[212:215], v144
	s_waitcnt lgkmcnt(1)
	v_smfmac_f32_16x16x64_f16 v[200:203], v[208:211], v[42:49], v191
	ds_read_b128 v[216:219], v145
	v_smfmac_f32_16x16x64_f16 v[204:207], v[208:211], v[74:81], v191
	ds_read_b128 v[220:223], v146
	s_waitcnt lgkmcnt(2)
	v_smfmac_f32_16x16x64_f16 v[200:203], v[212:215], v[50:57], v191
	v_smfmac_f32_16x16x64_f16 v[204:207], v[212:215], v[82:89], v191
	s_waitcnt lgkmcnt(1)
	v_smfmac_f32_16x16x64_f16 v[200:203], v[216:219], v[58:65], v191
	v_smfmac_f32_16x16x64_f16 v[204:207], v[216:219], v[90:97], v191
	s_waitcnt lgkmcnt(0)
	v_smfmac_f32_16x16x64_f16 v[200:203], v[220:223], v[66:73], v191
	v_smfmac_f32_16x16x64_f16 v[204:207], v[220:223], v[98:105], v191
	s_nop 6
	v_cndmask_b32_e64 v152, v201, v200, s[6:7]
	v_cndmask_b32_e64 v152, v152, v204, s[0:1]
	v_cndmask_b32_e64 v152, v152, v205, s[4:5]
	v_exp_f32_e32 v152, v152
	s_nop 0
	v_add_f32_e32 v152, 1.0, v152
	v_rcp_f32_e32 v152, v152
	s_nop 0
	v_fmac_f32_e32 v135, v152, v137
	s_nop 1
	v_add_f32_dpp v135, v135, v135 quad_perm:[1,0,3,2] row_mask:0xf bank_mask:0xf bound_ctrl:1
	s_nop 1
	v_add_f32_dpp v135, v135, v135 quad_perm:[2,3,0,1] row_mask:0xf bank_mask:0xf bound_ctrl:1
	s_nop 1
	v_add_f32_dpp v135, v135, v135 row_half_mirror row_mask:0xf bank_mask:0xf bound_ctrl:1
	v_cvt_f16_f32_e32 v137, v135
	ds_write_b16 v150, v137
	s_waitcnt lgkmcnt(0)
	s_barrier
	ds_read_b128 v[158:161], v147
	ds_read_b32 v137, v134 offset:32
	v_add_f32_e32 v135, v136, v135
	s_waitcnt lgkmcnt(1)
	v_smfmac_f32_16x16x64_f16 v[130:133], v[158:161], v[248:255], v191
	s_nop 7
	v_cndmask_b32_e64 v156, v130, v131, s[0:1]
	v_exp_f32_e64 v158, -|v156|
	v_max_f32 v159, 0, v156
	v_add_f32 v158, 1.0, v158
	v_log_f32 v158, v158
	s_nop 0
	v_fma_mixlo_f16 v157, v158, 1.0, v159
	ds_write_b16 v148, v157
	v_mov_b32_e32 v192, v106
	v_mov_b32_e32 v193, v110
	v_mul_f32 v136, -2.0, v137
	ds_read_b128 v[208:211], v139
	s_waitcnt lgkmcnt(1)
	s_barrier
	ds_read_b128 v[212:215], v140
	s_waitcnt lgkmcnt(1)
	v_smfmac_f32_16x16x64_f16 v[192:195], v[208:211], v[6:13], v191
	ds_read_b128 v[216:219], v141
	s_waitcnt lgkmcnt(1)
	v_smfmac_f32_16x16x64_f16 v[192:195], v[212:215], v[14:21], v191
	ds_read_b128 v[220:223], v142
	s_waitcnt lgkmcnt(1)
	v_smfmac_f32_16x16x64_f16 v[192:195], v[216:219], v[26:33], v191
	s_waitcnt lgkmcnt(0)
	v_smfmac_f32_16x16x64_f16 v[192:195], v[220:223], v[34:41], v191
	s_nop 7
	v_cndmask_b32_e64 v156, v192, v193, s[0:1]
	v_exp_f32_e64 v158, -|v156|
	v_max_f32 v159, 0, v156
	v_add_f32 v158, 1.0, v158
	v_log_f32 v158, v158
	s_nop 0
	v_fma_mixlo_f16 v157, v158, 1.0, v159
	ds_write_b16 v149, v157
	v_mov_b32_e32 v200, v114
	v_mov_b32_e32 v201, v118
	v_mov_b32_e32 v204, v122
	v_mov_b32_e32 v205, v126
	ds_read_b128 v[208:211], v143
	s_waitcnt lgkmcnt(1)
	s_barrier
	ds_read_b128 v[212:215], v144
	s_waitcnt lgkmcnt(1)
	v_smfmac_f32_16x16x64_f16 v[200:203], v[208:211], v[42:49], v191
	ds_read_b128 v[216:219], v145
	v_smfmac_f32_16x16x64_f16 v[204:207], v[208:211], v[74:81], v191
	ds_read_b128 v[220:223], v146
	s_waitcnt lgkmcnt(2)
	v_smfmac_f32_16x16x64_f16 v[200:203], v[212:215], v[50:57], v191
	v_smfmac_f32_16x16x64_f16 v[204:207], v[212:215], v[82:89], v191
	s_waitcnt lgkmcnt(1)
	v_smfmac_f32_16x16x64_f16 v[200:203], v[216:219], v[58:65], v191
	v_smfmac_f32_16x16x64_f16 v[204:207], v[216:219], v[90:97], v191
	s_waitcnt lgkmcnt(0)
	v_smfmac_f32_16x16x64_f16 v[200:203], v[220:223], v[66:73], v191
	v_smfmac_f32_16x16x64_f16 v[204:207], v[220:223], v[98:105], v191
	s_nop 6
	v_cndmask_b32_e64 v172, v201, v200, s[6:7]
	v_cndmask_b32_e64 v172, v172, v204, s[0:1]
	v_cndmask_b32_e64 v172, v172, v205, s[4:5]
	v_exp_f32_e32 v172, v172
	s_nop 0
	v_add_f32_e32 v172, 1.0, v172
	v_rcp_f32_e32 v172, v172
	s_nop 0
	v_fmac_f32_e32 v137, v172, v136
	s_nop 1
	v_add_f32_dpp v136, v137, v137 quad_perm:[1,0,3,2] row_mask:0xf bank_mask:0xf bound_ctrl:1
	s_nop 1
	v_add_f32_dpp v136, v136, v136 quad_perm:[2,3,0,1] row_mask:0xf bank_mask:0xf bound_ctrl:1
	s_nop 1
	v_add_f32_dpp v136, v136, v136 row_half_mirror row_mask:0xf bank_mask:0xf bound_ctrl:1
	v_cvt_f16_f32_e32 v137, v136
	ds_write_b16 v150, v137
	s_waitcnt lgkmcnt(0)
	s_barrier
	ds_read_b128 v[156:159], v147
	ds_read_b32 v137, v134 offset:64
	v_add_f32_e32 v135, v135, v136
	s_waitcnt lgkmcnt(1)
	v_smfmac_f32_16x16x64_f16 v[130:133], v[156:159], v[248:255], v191
	s_nop 7
	v_cndmask_b32_e64 v156, v130, v131, s[0:1]
	v_exp_f32_e64 v158, -|v156|
	v_max_f32 v159, 0, v156
	v_add_f32 v158, 1.0, v158
	v_log_f32 v158, v158
	s_nop 0
	v_fma_mixlo_f16 v157, v158, 1.0, v159
	ds_write_b16 v148, v157
	v_mov_b32_e32 v192, v106
	v_mov_b32_e32 v193, v110
	v_mul_f32 v136, -2.0, v137
	ds_read_b128 v[208:211], v139
	s_waitcnt lgkmcnt(1)
	s_barrier
	ds_read_b128 v[212:215], v140
	s_waitcnt lgkmcnt(1)
	v_smfmac_f32_16x16x64_f16 v[192:195], v[208:211], v[6:13], v191
	ds_read_b128 v[216:219], v141
	s_waitcnt lgkmcnt(1)
	v_smfmac_f32_16x16x64_f16 v[192:195], v[212:215], v[14:21], v191
	ds_read_b128 v[220:223], v142
	s_waitcnt lgkmcnt(1)
	v_smfmac_f32_16x16x64_f16 v[192:195], v[216:219], v[26:33], v191
	s_waitcnt lgkmcnt(0)
	v_smfmac_f32_16x16x64_f16 v[192:195], v[220:223], v[34:41], v191
	s_nop 7
	v_cndmask_b32_e64 v156, v192, v193, s[0:1]
	v_exp_f32_e64 v158, -|v156|
	v_max_f32 v159, 0, v156
	v_add_f32 v158, 1.0, v158
	v_log_f32 v158, v158
	s_nop 0
	v_fma_mixlo_f16 v157, v158, 1.0, v159
	ds_write_b16 v149, v157
	v_mov_b32_e32 v200, v114
	v_mov_b32_e32 v201, v118
	v_mov_b32_e32 v204, v122
	v_mov_b32_e32 v205, v126
	ds_read_b128 v[208:211], v143
	s_waitcnt lgkmcnt(1)
	s_barrier
	ds_read_b128 v[212:215], v144
	s_waitcnt lgkmcnt(1)
	v_smfmac_f32_16x16x64_f16 v[200:203], v[208:211], v[42:49], v191
	ds_read_b128 v[216:219], v145
	v_smfmac_f32_16x16x64_f16 v[204:207], v[208:211], v[74:81], v191
	ds_read_b128 v[220:223], v146
	s_waitcnt lgkmcnt(2)
	v_smfmac_f32_16x16x64_f16 v[200:203], v[212:215], v[50:57], v191
	v_smfmac_f32_16x16x64_f16 v[204:207], v[212:215], v[82:89], v191
	s_waitcnt lgkmcnt(1)
	v_smfmac_f32_16x16x64_f16 v[200:203], v[216:219], v[58:65], v191
	v_smfmac_f32_16x16x64_f16 v[204:207], v[216:219], v[90:97], v191
	s_waitcnt lgkmcnt(0)
	v_smfmac_f32_16x16x64_f16 v[200:203], v[220:223], v[66:73], v191
	v_smfmac_f32_16x16x64_f16 v[204:207], v[220:223], v[98:105], v191
	s_nop 6
	v_cndmask_b32_e64 v172, v201, v200, s[6:7]
	v_cndmask_b32_e64 v172, v172, v204, s[0:1]
	v_cndmask_b32_e64 v172, v172, v205, s[4:5]
	v_exp_f32_e32 v172, v172
	s_nop 0
	v_add_f32_e32 v172, 1.0, v172
	v_rcp_f32_e32 v172, v172
	s_nop 0
	v_fmac_f32_e32 v137, v172, v136
	s_nop 1
	v_add_f32_dpp v136, v137, v137 quad_perm:[1,0,3,2] row_mask:0xf bank_mask:0xf bound_ctrl:1
	s_nop 1
	v_add_f32_dpp v136, v136, v136 quad_perm:[2,3,0,1] row_mask:0xf bank_mask:0xf bound_ctrl:1
	s_nop 1
	v_add_f32_dpp v136, v136, v136 row_half_mirror row_mask:0xf bank_mask:0xf bound_ctrl:1
	v_cvt_f16_f32_e32 v137, v136
	ds_write_b16 v150, v137
	s_waitcnt lgkmcnt(0)
	s_barrier
	ds_read_b128 v[156:159], v147
	ds_read_b32 v137, v134 offset:96
	v_add_f32_e32 v135, v135, v136
	s_waitcnt lgkmcnt(1)
	v_smfmac_f32_16x16x64_f16 v[130:133], v[156:159], v[248:255], v191
	s_nop 7
	v_cndmask_b32_e64 v156, v130, v131, s[0:1]
	v_exp_f32_e64 v158, -|v156|
	v_max_f32 v159, 0, v156
	v_add_f32 v158, 1.0, v158
	v_log_f32 v158, v158
	s_nop 0
	v_fma_mixlo_f16 v157, v158, 1.0, v159
	ds_write_b16 v148, v157
	v_mov_b32_e32 v192, v106
	v_mov_b32_e32 v193, v110
	v_mul_f32 v136, -2.0, v137
	ds_read_b128 v[208:211], v139
	s_waitcnt lgkmcnt(1)
	s_barrier
	ds_read_b128 v[212:215], v140
	s_waitcnt lgkmcnt(1)
	v_smfmac_f32_16x16x64_f16 v[192:195], v[208:211], v[6:13], v191
	ds_read_b128 v[216:219], v141
	s_waitcnt lgkmcnt(1)
	v_smfmac_f32_16x16x64_f16 v[192:195], v[212:215], v[14:21], v191
	ds_read_b128 v[220:223], v142
	s_waitcnt lgkmcnt(1)
	v_smfmac_f32_16x16x64_f16 v[192:195], v[216:219], v[26:33], v191
	s_waitcnt lgkmcnt(0)
	v_smfmac_f32_16x16x64_f16 v[192:195], v[220:223], v[34:41], v191
	s_nop 7
	v_cndmask_b32_e64 v156, v192, v193, s[0:1]
	v_exp_f32_e64 v158, -|v156|
	v_max_f32 v159, 0, v156
	v_add_f32 v158, 1.0, v158
	v_log_f32 v158, v158
	s_nop 0
	v_fma_mixlo_f16 v157, v158, 1.0, v159
	ds_write_b16 v149, v157
	v_mov_b32_e32 v200, v114
	v_mov_b32_e32 v201, v118
	v_mov_b32_e32 v204, v122
	v_mov_b32_e32 v205, v126
	ds_read_b128 v[208:211], v143
	s_waitcnt lgkmcnt(1)
	s_barrier
	ds_read_b128 v[212:215], v144
	s_waitcnt lgkmcnt(1)
	v_smfmac_f32_16x16x64_f16 v[200:203], v[208:211], v[42:49], v191
	ds_read_b128 v[216:219], v145
	v_smfmac_f32_16x16x64_f16 v[204:207], v[208:211], v[74:81], v191
	ds_read_b128 v[220:223], v146
	s_waitcnt lgkmcnt(2)
	v_smfmac_f32_16x16x64_f16 v[200:203], v[212:215], v[50:57], v191
	v_smfmac_f32_16x16x64_f16 v[204:207], v[212:215], v[82:89], v191
	s_waitcnt lgkmcnt(1)
	v_smfmac_f32_16x16x64_f16 v[200:203], v[216:219], v[58:65], v191
	v_smfmac_f32_16x16x64_f16 v[204:207], v[216:219], v[90:97], v191
	s_waitcnt lgkmcnt(0)
	v_smfmac_f32_16x16x64_f16 v[200:203], v[220:223], v[66:73], v191
	v_smfmac_f32_16x16x64_f16 v[204:207], v[220:223], v[98:105], v191
	s_nop 6
	v_cndmask_b32_e64 v172, v201, v200, s[6:7]
	v_cndmask_b32_e64 v172, v172, v204, s[0:1]
	v_cndmask_b32_e64 v172, v172, v205, s[4:5]
	v_exp_f32_e32 v172, v172
	s_nop 0
	v_add_f32_e32 v172, 1.0, v172
	v_rcp_f32_e32 v172, v172
	s_nop 0
	v_fmac_f32_e32 v137, v172, v136
	s_nop 1
	v_add_f32_dpp v136, v137, v137 quad_perm:[1,0,3,2] row_mask:0xf bank_mask:0xf bound_ctrl:1
	s_nop 1
	v_add_f32_dpp v136, v136, v136 quad_perm:[2,3,0,1] row_mask:0xf bank_mask:0xf bound_ctrl:1
	s_nop 1
	v_add_f32_dpp v136, v136, v136 row_half_mirror row_mask:0xf bank_mask:0xf bound_ctrl:1
	v_cvt_f16_f32_e32 v137, v136
	ds_write_b16 v150, v137
	s_waitcnt lgkmcnt(0)
	s_barrier
	ds_read_b128 v[156:159], v147
	ds_read_b32 v137, v134 offset:128
	v_add_f32_e32 v135, v135, v136
	s_waitcnt lgkmcnt(1)
	v_smfmac_f32_16x16x64_f16 v[130:133], v[156:159], v[248:255], v191
	s_nop 7
	v_cndmask_b32_e64 v156, v130, v131, s[0:1]
	v_exp_f32_e64 v158, -|v156|
	v_max_f32 v159, 0, v156
	v_add_f32 v158, 1.0, v158
	v_log_f32 v158, v158
	s_nop 0
	v_fma_mixlo_f16 v157, v158, 1.0, v159
	ds_write_b16 v148, v157
	v_mov_b32_e32 v192, v106
	v_mov_b32_e32 v193, v110
	v_mul_f32 v136, -2.0, v137
	ds_read_b128 v[208:211], v139
	s_waitcnt lgkmcnt(1)
	s_barrier
	ds_read_b128 v[212:215], v140
	s_waitcnt lgkmcnt(1)
	v_smfmac_f32_16x16x64_f16 v[192:195], v[208:211], v[6:13], v191
	ds_read_b128 v[216:219], v141
	s_waitcnt lgkmcnt(1)
	v_smfmac_f32_16x16x64_f16 v[192:195], v[212:215], v[14:21], v191
	ds_read_b128 v[220:223], v142
	s_waitcnt lgkmcnt(1)
	v_smfmac_f32_16x16x64_f16 v[192:195], v[216:219], v[26:33], v191
	s_waitcnt lgkmcnt(0)
	v_smfmac_f32_16x16x64_f16 v[192:195], v[220:223], v[34:41], v191
	s_nop 7
	v_cndmask_b32_e64 v156, v192, v193, s[0:1]
	v_exp_f32_e64 v158, -|v156|
	v_max_f32 v159, 0, v156
	v_add_f32 v158, 1.0, v158
	v_log_f32 v158, v158
	s_nop 0
	v_fma_mixlo_f16 v157, v158, 1.0, v159
	ds_write_b16 v149, v157
	v_mov_b32_e32 v200, v114
	v_mov_b32_e32 v201, v118
	v_mov_b32_e32 v204, v122
	v_mov_b32_e32 v205, v126
	ds_read_b128 v[208:211], v143
	s_waitcnt lgkmcnt(1)
	s_barrier
	ds_read_b128 v[212:215], v144
	s_waitcnt lgkmcnt(1)
	v_smfmac_f32_16x16x64_f16 v[200:203], v[208:211], v[42:49], v191
	ds_read_b128 v[216:219], v145
	v_smfmac_f32_16x16x64_f16 v[204:207], v[208:211], v[74:81], v191
	ds_read_b128 v[220:223], v146
	s_waitcnt lgkmcnt(2)
	v_smfmac_f32_16x16x64_f16 v[200:203], v[212:215], v[50:57], v191
	v_smfmac_f32_16x16x64_f16 v[204:207], v[212:215], v[82:89], v191
	s_waitcnt lgkmcnt(1)
	v_smfmac_f32_16x16x64_f16 v[200:203], v[216:219], v[58:65], v191
	v_smfmac_f32_16x16x64_f16 v[204:207], v[216:219], v[90:97], v191
	s_waitcnt lgkmcnt(0)
	v_smfmac_f32_16x16x64_f16 v[200:203], v[220:223], v[66:73], v191
	v_smfmac_f32_16x16x64_f16 v[204:207], v[220:223], v[98:105], v191
	s_nop 6
	v_cndmask_b32_e64 v172, v201, v200, s[6:7]
	v_cndmask_b32_e64 v172, v172, v204, s[0:1]
	v_cndmask_b32_e64 v172, v172, v205, s[4:5]
	v_exp_f32_e32 v172, v172
	s_nop 0
	v_add_f32_e32 v172, 1.0, v172
	v_rcp_f32_e32 v172, v172
	s_nop 0
	v_fmac_f32_e32 v137, v172, v136
	s_nop 1
	v_add_f32_dpp v136, v137, v137 quad_perm:[1,0,3,2] row_mask:0xf bank_mask:0xf bound_ctrl:1
	s_nop 1
	v_add_f32_dpp v136, v136, v136 quad_perm:[2,3,0,1] row_mask:0xf bank_mask:0xf bound_ctrl:1
	s_nop 1
	v_add_f32_dpp v136, v136, v136 row_half_mirror row_mask:0xf bank_mask:0xf bound_ctrl:1
	v_cvt_f16_f32_e32 v137, v136
	ds_write_b16 v150, v137
	s_waitcnt lgkmcnt(0)
	s_barrier
	ds_read_b128 v[156:159], v147
	ds_read_b32 v137, v134 offset:160
	v_add_f32_e32 v135, v135, v136
	s_waitcnt lgkmcnt(1)
	v_smfmac_f32_16x16x64_f16 v[130:133], v[156:159], v[248:255], v191
	s_nop 7
	v_cndmask_b32_e64 v156, v130, v131, s[0:1]
	v_exp_f32_e64 v158, -|v156|
	v_max_f32 v159, 0, v156
	v_add_f32 v158, 1.0, v158
	v_log_f32 v158, v158
	s_nop 0
	v_fma_mixlo_f16 v157, v158, 1.0, v159
	ds_write_b16 v148, v157
	v_mov_b32_e32 v192, v106
	v_mov_b32_e32 v193, v110
	v_mul_f32 v136, -2.0, v137
	ds_read_b128 v[208:211], v139
	s_waitcnt lgkmcnt(1)
	s_barrier
	ds_read_b128 v[212:215], v140
	s_waitcnt lgkmcnt(1)
	v_smfmac_f32_16x16x64_f16 v[192:195], v[208:211], v[6:13], v191
	ds_read_b128 v[216:219], v141
	s_waitcnt lgkmcnt(1)
	v_smfmac_f32_16x16x64_f16 v[192:195], v[212:215], v[14:21], v191
	ds_read_b128 v[220:223], v142
	s_waitcnt lgkmcnt(1)
	v_smfmac_f32_16x16x64_f16 v[192:195], v[216:219], v[26:33], v191
	s_waitcnt lgkmcnt(0)
	v_smfmac_f32_16x16x64_f16 v[192:195], v[220:223], v[34:41], v191
	s_nop 7
	v_cndmask_b32_e64 v156, v192, v193, s[0:1]
	v_exp_f32_e64 v158, -|v156|
	v_max_f32 v159, 0, v156
	v_add_f32 v158, 1.0, v158
	v_log_f32 v158, v158
	s_nop 0
	v_fma_mixlo_f16 v157, v158, 1.0, v159
	ds_write_b16 v149, v157
	v_mov_b32_e32 v200, v114
	v_mov_b32_e32 v201, v118
	v_mov_b32_e32 v204, v122
	v_mov_b32_e32 v205, v126
	ds_read_b128 v[208:211], v143
	s_waitcnt lgkmcnt(1)
	s_barrier
	ds_read_b128 v[212:215], v144
	s_waitcnt lgkmcnt(1)
	v_smfmac_f32_16x16x64_f16 v[200:203], v[208:211], v[42:49], v191
	ds_read_b128 v[216:219], v145
	v_smfmac_f32_16x16x64_f16 v[204:207], v[208:211], v[74:81], v191
	ds_read_b128 v[220:223], v146
	s_waitcnt lgkmcnt(2)
	v_smfmac_f32_16x16x64_f16 v[200:203], v[212:215], v[50:57], v191
	v_smfmac_f32_16x16x64_f16 v[204:207], v[212:215], v[82:89], v191
	s_waitcnt lgkmcnt(1)
	v_smfmac_f32_16x16x64_f16 v[200:203], v[216:219], v[58:65], v191
	v_smfmac_f32_16x16x64_f16 v[204:207], v[216:219], v[90:97], v191
	s_waitcnt lgkmcnt(0)
	v_smfmac_f32_16x16x64_f16 v[200:203], v[220:223], v[66:73], v191
	v_smfmac_f32_16x16x64_f16 v[204:207], v[220:223], v[98:105], v191
	s_nop 6
	v_cndmask_b32_e64 v172, v201, v200, s[6:7]
	v_cndmask_b32_e64 v172, v172, v204, s[0:1]
	v_cndmask_b32_e64 v172, v172, v205, s[4:5]
	v_exp_f32_e32 v172, v172
	s_nop 0
	v_add_f32_e32 v172, 1.0, v172
	v_rcp_f32_e32 v172, v172
	s_nop 0
	v_fmac_f32_e32 v137, v172, v136
	s_nop 1
	v_add_f32_dpp v136, v137, v137 quad_perm:[1,0,3,2] row_mask:0xf bank_mask:0xf bound_ctrl:1
	s_nop 1
	v_add_f32_dpp v136, v136, v136 quad_perm:[2,3,0,1] row_mask:0xf bank_mask:0xf bound_ctrl:1
	s_nop 1
	v_add_f32_dpp v136, v136, v136 row_half_mirror row_mask:0xf bank_mask:0xf bound_ctrl:1
	v_cvt_f16_f32_e32 v137, v136
	ds_write_b16 v150, v137
	s_waitcnt lgkmcnt(0)
	s_barrier
	ds_read_b128 v[156:159], v147
	ds_read_b32 v137, v134 offset:192
	v_add_f32_e32 v135, v135, v136
	s_waitcnt lgkmcnt(1)
	v_smfmac_f32_16x16x64_f16 v[130:133], v[156:159], v[248:255], v191
	s_nop 7
	v_cndmask_b32_e64 v152, v130, v131, s[0:1]
	v_exp_f32_e64 v158, -|v152|
	v_max_f32 v159, 0, v152
	v_add_f32 v158, 1.0, v158
	v_log_f32 v158, v158
	s_nop 0
	v_fma_mixlo_f16 v153, v158, 1.0, v159
	ds_write_b16 v148, v153
	v_mov_b32_e32 v192, v106
	v_mov_b32_e32 v193, v110
	v_mul_f32 v136, -2.0, v137
	ds_read_b128 v[208:211], v139
	s_waitcnt lgkmcnt(1)
	s_barrier
	ds_read_b128 v[212:215], v140
	s_waitcnt lgkmcnt(1)
	v_smfmac_f32_16x16x64_f16 v[192:195], v[208:211], v[6:13], v191
	ds_read_b128 v[216:219], v141
	s_waitcnt lgkmcnt(1)
	v_smfmac_f32_16x16x64_f16 v[192:195], v[212:215], v[14:21], v191
	ds_read_b128 v[220:223], v142
	s_waitcnt lgkmcnt(1)
	v_smfmac_f32_16x16x64_f16 v[192:195], v[216:219], v[26:33], v191
	s_waitcnt lgkmcnt(0)
	v_smfmac_f32_16x16x64_f16 v[192:195], v[220:223], v[34:41], v191
	s_nop 7
	v_cndmask_b32_e64 v152, v192, v193, s[0:1]
	v_exp_f32_e64 v158, -|v152|
	v_max_f32 v159, 0, v152
	v_add_f32 v158, 1.0, v158
	v_log_f32 v158, v158
	s_nop 0
	v_fma_mixlo_f16 v153, v158, 1.0, v159
	ds_write_b16 v149, v153
	v_mov_b32_e32 v200, v114
	v_mov_b32_e32 v201, v118
	v_mov_b32_e32 v204, v122
	v_mov_b32_e32 v205, v126
	ds_read_b128 v[208:211], v143
	s_waitcnt lgkmcnt(1)
	s_barrier
	ds_read_b128 v[212:215], v144
	s_waitcnt lgkmcnt(1)
	v_smfmac_f32_16x16x64_f16 v[200:203], v[208:211], v[42:49], v191
	ds_read_b128 v[216:219], v145
	v_smfmac_f32_16x16x64_f16 v[204:207], v[208:211], v[74:81], v191
	ds_read_b128 v[220:223], v146
	s_waitcnt lgkmcnt(2)
	v_smfmac_f32_16x16x64_f16 v[200:203], v[212:215], v[50:57], v191
	v_smfmac_f32_16x16x64_f16 v[204:207], v[212:215], v[82:89], v191
	s_waitcnt lgkmcnt(1)
	v_smfmac_f32_16x16x64_f16 v[200:203], v[216:219], v[58:65], v191
	v_smfmac_f32_16x16x64_f16 v[204:207], v[216:219], v[90:97], v191
	s_waitcnt lgkmcnt(0)
	v_smfmac_f32_16x16x64_f16 v[200:203], v[220:223], v[66:73], v191
	v_smfmac_f32_16x16x64_f16 v[204:207], v[220:223], v[98:105], v191
	s_nop 6
	v_cndmask_b32_e64 v152, v201, v200, s[6:7]
	v_cndmask_b32_e64 v152, v152, v204, s[0:1]
	v_cndmask_b32_e64 v152, v152, v205, s[4:5]
	v_exp_f32_e32 v152, v152
	s_nop 0
	v_add_f32_e32 v152, 1.0, v152
	v_rcp_f32_e32 v152, v152
	s_nop 0
	v_fmac_f32_e32 v137, v152, v136
	s_nop 1
	v_add_f32_dpp v136, v137, v137 quad_perm:[1,0,3,2] row_mask:0xf bank_mask:0xf bound_ctrl:1
	s_nop 1
	v_add_f32_dpp v136, v136, v136 quad_perm:[2,3,0,1] row_mask:0xf bank_mask:0xf bound_ctrl:1
	s_nop 1
	v_add_f32_dpp v136, v136, v136 row_half_mirror row_mask:0xf bank_mask:0xf bound_ctrl:1
	v_cvt_f16_f32_e32 v137, v136
	ds_write_b16 v150, v137
	s_waitcnt lgkmcnt(0)
	s_barrier
	ds_read_b128 v[158:161], v147
	v_add_f32_e32 v152, v135, v136
	ds_read_b32 v153, v134 offset:224
	s_addk_i32 s3, 0x100
	s_cmpk_eq_u32 s3, 0xfa20
	s_waitcnt lgkmcnt(1)
	v_smfmac_f32_16x16x64_f16 v[130:133], v[158:161], v[248:255], v191
	s_nop 7
	v_cndmask_b32_e64 v154, v130, v131, s[0:1]
	s_cbranch_scc0 .LBB0_21
	s_and_saveexec_b64 s[0:1], vcc
	ds_write_b32 v1, v152
	s_or_b64 exec, exec, s[0:1]
	v_cmp_gt_u32_e32 vcc, 10, v0
	s_waitcnt lgkmcnt(0)
	s_barrier
	s_and_saveexec_b64 s[0:1], vcc
	s_cbranch_execz .LBB0_28
	v_lshlrev_b32_e32 v1, 2, v0
	global_load_dword v1, v1, s[12:13]
	v_mov_b32_e32 v139, 0
	v_lshl_add_u64 v[2:3], s[10:11], 0, v[138:139]
	v_lshl_add_u64 v[2:3], v[2:3], 0, 28
	s_mov_b32 s0, 0

	.amdhsa_kernel _Z11ncde_kernelPKfS0_S0_S0_S0_S0_S0_S0_S0_S0_S0_S0_S0_S0_S0_S0_S0_S0_S0_Pf
		.amdhsa_group_segment_fixed_size 79040
		.amdhsa_private_segment_fixed_size 0
		.amdhsa_kernarg_size 160
		.amdhsa_user_sgpr_count 2
		.amdhsa_user_sgpr_dispatch_ptr 0
		.amdhsa_user_sgpr_queue_ptr 0
		.amdhsa_user_sgpr_kernarg_segment_ptr 1
		.amdhsa_user_sgpr_dispatch_id 0
		.amdhsa_user_sgpr_kernarg_preload_length 0
		.amdhsa_user_sgpr_kernarg_preload_offset 0
		.amdhsa_user_sgpr_private_segment_size 0
		.amdhsa_uses_dynamic_stack 0
		.amdhsa_enable_private_segment 0
		.amdhsa_system_sgpr_workgroup_id_x 1
		.amdhsa_system_sgpr_workgroup_id_y 0
		.amdhsa_system_sgpr_workgroup_id_z 0
		.amdhsa_system_sgpr_workgroup_info 0
		.amdhsa_system_vgpr_workitem_id 0
		.amdhsa_next_free_vgpr 256
		.amdhsa_next_free_sgpr 96
		.amdhsa_accum_offset 256
		.amdhsa_reserve_vcc 1
		.amdhsa_float_round_mode_32 0
		.amdhsa_float_round_mode_16_64 0
		.amdhsa_float_denorm_mode_32 3
		.amdhsa_float_denorm_mode_16_64 3
		.amdhsa_dx10_clamp 1
		.amdhsa_ieee_mode 1
		.amdhsa_fp16_overflow 0
		.amdhsa_tg_split 0
		.amdhsa_exception_fp_ieee_invalid_op 0
		.amdhsa_exception_fp_denorm_src 0
		.amdhsa_exception_fp_ieee_div_zero 0
		.amdhsa_exception_fp_ieee_overflow 0
		.amdhsa_exception_fp_ieee_underflow 0
		.amdhsa_exception_fp_ieee_inexact 0
		.amdhsa_exception_int_div_zero 0
	.end_amdhsa_kernel

amdhsa.kernels:
  - .agpr_count:     0
    .args:
      - .actual_access:  read_only
        .address_space:  global
        .offset:         0
        .size:           8
        .value_kind:     global_buffer
      - .actual_access:  read_only
        .address_space:  global
        .offset:         8
        .size:           8
        .value_kind:     global_buffer
      - .actual_access:  read_only
        .address_space:  global
        .offset:         16
        .size:           8
        .value_kind:     global_buffer
      - .actual_access:  read_only
        .address_space:  global
        .offset:         24
        .size:           8
        .value_kind:     global_buffer
      - .actual_access:  read_only
        .address_space:  global
        .offset:         32
        .size:           8
        .value_kind:     global_buffer
      - .actual_access:  read_only
        .address_space:  global
        .offset:         40
        .size:           8
        .value_kind:     global_buffer
      - .actual_access:  read_only
        .address_space:  global
        .offset:         48
        .size:           8
        .value_kind:     global_buffer
      - .actual_access:  read_only
        .address_space:  global
        .offset:         56
        .size:           8
        .value_kind:     global_buffer
      - .actual_access:  read_only
        .address_space:  global
        .offset:         64
        .size:           8
        .value_kind:     global_buffer
      - .actual_access:  read_only
        .address_space:  global
        .offset:         72
        .size:           8
        .value_kind:     global_buffer
      - .actual_access:  read_only
        .address_space:  global
        .offset:         80
        .size:           8
        .value_kind:     global_buffer
      - .actual_access:  read_only
        .address_space:  global
        .offset:         88
        .size:           8
        .value_kind:     global_buffer
      - .actual_access:  read_only
        .address_space:  global
        .offset:         96
        .size:           8
        .value_kind:     global_buffer
      - .actual_access:  read_only
        .address_space:  global
        .offset:         104
        .size:           8
        .value_kind:     global_buffer
      - .actual_access:  read_only
        .address_space:  global
        .offset:         112
        .size:           8
        .value_kind:     global_buffer
      - .actual_access:  read_only
        .address_space:  global
        .offset:         120
        .size:           8
        .value_kind:     global_buffer
      - .actual_access:  read_only
        .address_space:  global
        .offset:         128
        .size:           8
        .value_kind:     global_buffer
      - .actual_access:  read_only
        .address_space:  global
        .offset:         136
        .size:           8
        .value_kind:     global_buffer
      - .actual_access:  read_only
        .address_space:  global
        .offset:         144
        .size:           8
        .value_kind:     global_buffer
      - .actual_access:  write_only
        .address_space:  global
        .offset:         152
        .size:           8
        .value_kind:     global_buffer
    .group_segment_fixed_size: 79040
    .kernarg_segment_align: 8
    .kernarg_segment_size: 160
    .language:       OpenCL C
    .language_version:
      - 2
      - 0
    .max_flat_workgroup_size: 256
    .name:           _Z11ncde_kernelPKfS0_S0_S0_S0_S0_S0_S0_S0_S0_S0_S0_S0_S0_S0_S0_S0_S0_S0_Pf
    .private_segment_fixed_size: 0
    .sgpr_count:     50
    .sgpr_spill_count: 0
    .symbol:         _Z11ncde_kernelPKfS0_S0_S0_S0_S0_S0_S0_S0_S0_S0_S0_S0_S0_S0_S0_S0_S0_S0_Pf.kd
    .uniform_work_group_size: 1
    .uses_dynamic_stack: false
    .vgpr_count:     256
    .vgpr_spill_count: 0
    .wavefront_size: 64
